# P0 fp8 conversion loop: the 16 serialized gain loads per item replaced by 4 dwordx4 loads issued before the next tile DMA (covered by the existing vmcnt(8))
# baseline (speedup 1.0000x reference)
.LBB0_45:
	s_add_u32 s0, s24, 0x2400000
	s_addc_u32 s1, s25, 0
	v_lshlrev_b32_e32 v1, 4, v82
	s_add_u32 s30, s24, 0xa400000
	v_lshrrev_b32_e32 v8, 2, v0
	v_and_b32_e32 v12, 48, v1
	s_addc_u32 s31, s25, 0
	v_lshrrev_b32_e32 v1, 1, v82
	v_and_b32_e32 v4, 3, v82
	s_movk_i32 s2, 0x840
	v_mov_b32_e32 v3, s7
	v_mov_b32_e32 v5, 0
	v_lshlrev_b32_e32 v6, 10, v8
	v_or_b32_e32 v8, 16, v8
	s_add_i32 s27, s27, s34
	v_and_b32_e32 v1, 28, v1
	v_and_b32_e32 v2, 0x70, v66
	v_mad_u32_u24 v3, v4, s2, v3
	v_lshlrev_b32_e32 v4, 4, v4
	v_and_b32_e32 v10, 60, v82
	v_mov_b32_e32 v7, v5
	v_lshlrev_b32_e32 v11, 2, v8
	v_lshlrev_b32_e32 v8, 10, v8
	v_mov_b32_e32 v9, v5
	s_sub_i32 s33, s27, s26
	s_mov_b32 s5, 0
	s_mov_b32 s11, 0x20000
	s_brev_b32 s10, -2
	v_lshlrev_b32_e32 v12, 2, v12
	s_mov_b32 s4, 0
	s_cmp_eq_u64 s[14:15], 0
	s_cbranch_scc1 .Lp0g_skip0
	s_nop 0
	global_load_dwordx4 v[160:163], v12, s[14:15]
	global_load_dwordx4 v[164:167], v12, s[14:15] offset:16
	global_load_dwordx4 v[168:171], v12, s[14:15] offset:32
	global_load_dwordx4 v[172:175], v12, s[14:15] offset:48
	s_waitcnt vmcnt(0)

.LBB0_46:
	s_lshr_b32 s41, s4, 5
	s_sext_i32_i16 s29, s40
	v_cvt_f32_ubyte0_e32 v30, s41
	v_cvt_f32_i32_e32 v29, s29
	v_rcp_iflag_f32_e32 v31, v30
	s_xor_b32 s28, s39, 1
	s_mulk_i32 s28, 0x2100
	s_add_i32 s44, s7, s28
	v_mul_f32_e32 v31, v29, v31
	v_trunc_f32_e32 v31, v31
	v_fma_f32 v29, -v31, v30, v29
	v_cvt_i32_f32_e32 v31, v31
	s_ashr_i32 s28, s29, 30
	s_or_b32 s42, s28, 1
	v_cmp_ge_f32_e64 s[28:29], |v29|, v30
	s_and_b64 s[28:29], s[28:29], exec
	s_cselect_b32 s28, s42, 0
	v_readfirstlane_b32 s29, v31
	s_add_i32 s28, s29, s28
	s_sext_i32_i16 s29, s28
	s_mul_i32 s28, s28, s41
	s_sub_i32 s28, s40, s28
	s_sext_i32_i16 s41, s28
	s_lshl_b32 s28, s29, 6
	s_lshl_b32 s40, s41, 5
	s_lshl_b32 s29, s41, 6
	s_lshl_b32 s41, s41, 2
	s_and_b32 s29, s29, 0x700
	s_and_b32 s41, s41, 0xffffff80
	s_add_i32 s29, s29, s41
	s_and_b32 s41, s40, 0x60
	s_or_b32 s29, s29, s41
	s_and_b64 s[2:3], exec, s[2:3]
	s_mul_hi_i32 s43, s28, s4
	s_mul_i32 s42, s28, s4
	s_cselect_b32 s2, s40, s29
	s_ashr_i32 s29, s28, 31
	s_lshl_b64 s[42:43], s[42:43], 2
	s_add_u32 s3, s8, s42
	s_addc_u32 s42, s9, s43
	s_ashr_i32 s41, s40, 31
	s_lshl_b64 s[8:9], s[40:41], 2
	s_add_u32 s8, s3, s8
	s_addc_u32 s9, s42, s9
	s_ashr_i32 s3, s2, 31
	s_lshl_b64 s[2:3], s[2:3], 10
	s_add_u32 s2, s26, s2
	s_addc_u32 s3, s27, s3
	s_add_u32 s2, s2, s28
	s_addc_u32 s3, s3, s29
	s_lshl_b64 s[26:27], s[28:29], 2
	s_add_u32 s26, s14, s26
	s_addc_u32 s27, s15, s27
	s_cmp_lg_u64 s[14:15], 0
	s_cselect_b32 s15, s27, 0
	s_cselect_b32 s14, s26, 0
	s_cbranch_scc0 .Lp0g_skipn
	global_load_dwordx4 v[160:163], v12, s[14:15]
	global_load_dwordx4 v[164:167], v12, s[14:15] offset:16
	global_load_dwordx4 v[168:171], v12, s[14:15] offset:32
	global_load_dwordx4 v[172:175], v12, s[14:15] offset:48
.Lp0g_skipn:
	s_and_b32 s9, s9, 0xffff
	v_mad_u64_u32 v[30:31], s[26:27], s4, v1, v[2:3]
	s_mov_b32 m0, s44
	s_lshl_b32 s26, s4, 5
	buffer_load_dwordx4 v30, s[8:11], 0 offen lds
	s_add_i32 m0, s44, 0x400
	s_nop 0
	buffer_load_dwordx4 v30, s[8:11], s26 offen lds
	s_add_i32 m0, s44, 0x840
	s_lshl_b32 s26, s4, 6
	buffer_load_dwordx4 v30, s[8:11], s26 offen lds
	s_add_i32 m0, s44, 0xc40
	s_mul_i32 s26, s4, 0x60
	buffer_load_dwordx4 v30, s[8:11], s26 offen lds
	s_add_i32 m0, s44, 0x1080
	s_lshl_b32 s26, s4, 7
	buffer_load_dwordx4 v30, s[8:11], s26 offen lds
	s_add_i32 m0, s44, 0x1480
	s_mul_i32 s26, s4, 0xa0
	buffer_load_dwordx4 v30, s[8:11], s26 offen lds
	s_add_i32 m0, s44, 0x18c0
	s_mul_i32 s26, s4, 0xc0
	buffer_load_dwordx4 v30, s[8:11], s26 offen lds
	s_add_i32 m0, s44, 0x1cc0
	s_mulk_i32 s4, 0xe0
	buffer_load_dwordx4 v30, s[8:11], s4 offen lds
	s_waitcnt vmcnt(8)

.LBB0_48:
	s_cmp_eq_u64 s[14:15], 0
	v_mov_b32_e32 v13, 0x42800000
	v_mov_b32_e32 v14, 0x42800000
	v_mov_b32_e32 v15, 0x42800000
	v_mov_b32_e32 v16, 0x42800000
	v_mov_b32_e32 v17, 0x42800000
	v_mov_b32_e32 v18, 0x42800000
	v_mov_b32_e32 v19, 0x42800000
	v_mov_b32_e32 v20, 0x42800000
	v_mov_b32_e32 v21, 0x42800000
	v_mov_b32_e32 v22, 0x42800000
	v_mov_b32_e32 v23, 0x42800000
	v_mov_b32_e32 v24, 0x42800000
	v_mov_b32_e32 v25, 0x42800000
	v_mov_b32_e32 v26, 0x42800000
	v_mov_b32_e32 v27, 0x42800000
	v_mov_b32_e32 v28, 0x42800000
	s_cbranch_scc1 .LBB0_80
	v_mul_f32_e32 v14, 0x42800000, v160
	v_mul_f32_e32 v13, 0x42800000, v161
	v_mul_f32_e32 v16, 0x42800000, v162
	v_mul_f32_e32 v15, 0x42800000, v163
	v_mul_f32_e32 v18, 0x42800000, v164
	v_mul_f32_e32 v17, 0x42800000, v165
	v_mul_f32_e32 v20, 0x42800000, v166
	v_mul_f32_e32 v19, 0x42800000, v167
	v_mul_f32_e32 v22, 0x42800000, v168
	v_mul_f32_e32 v21, 0x42800000, v169
	v_mul_f32_e32 v24, 0x42800000, v170
	v_mul_f32_e32 v23, 0x42800000, v171
	v_mul_f32_e32 v26, 0x42800000, v172
	v_mul_f32_e32 v25, 0x42800000, v173
	v_mul_f32_e32 v28, 0x42800000, v174
	v_mul_f32_e32 v27, 0x42800000, v175
